# grid barrier: L1 invalidate (acquire) issued at arrival, overlapping the arrival atomic and the spin, instead of after the release flag
# speedup vs baseline: 1.0725x; 1.0155x over previous
.LBB0_80:
	s_or_b64 exec, exec, s[8:9]
	buffer_inv sc1
	v_cvt_f32_u32_e32 v6, v4
	s_waitcnt vmcnt(0)
	v_readfirstlane_b32 s0, v5
	v_sub_u32_e32 v5, 0, v4
	v_rcp_iflag_f32_e32 v6, v6
	v_add_u32_e32 v7, s0, v3
	v_mul_f32_e32 v6, 0x4f7ffffe, v6
	v_cvt_u32_f32_e32 v6, v6
	v_mul_lo_u32 v3, v5, v6
	v_mul_hi_u32 v3, v6, v3
	v_add_u32_e32 v3, v6, v3
	v_mul_hi_u32 v3, v7, v3
	v_mul_lo_u32 v5, v3, v4
	v_sub_u32_e32 v5, v7, v5
	v_add_u32_e32 v6, 1, v3
	v_sub_u32_e32 v8, v5, v4
	v_cmp_ge_u32_e32 vcc, v5, v4
	s_nop 1
	v_cndmask_b32_e32 v3, v3, v6, vcc
	v_cndmask_b32_e32 v5, v5, v8, vcc
	v_add_u32_e32 v6, 1, v3
	v_cmp_ge_u32_e32 vcc, v5, v4
	v_add_u32_e32 v5, 1, v7
	s_nop 0
	v_cndmask_b32_e32 v3, v3, v6, vcc
	v_mul_lo_u32 v6, v4, v3
	v_add_u32_e32 v4, v6, v4
	v_cmp_ne_u32_e32 vcc, v5, v4
	s_and_saveexec_b64 s[0:1], vcc
	s_xor_b64 s[0:1], exec, s[0:1]
	s_cbranch_execz .LBB0_94
	s_waitcnt lgkmcnt(0)
	global_load_dword v2, v199, s[6:7] offset:1024 sc1
	s_add_u32 s10, s6, 0x2400
	s_addc_u32 s11, s7, 0
	s_waitcnt vmcnt(0)
	v_cmp_eq_u32_e32 vcc, v2, v3
	s_and_saveexec_b64 s[8:9], vcc
	s_cbranch_execz .LBB0_93
	s_mov_b32 s22, 1
	s_mov_b64 s[12:13], 0
	s_branch .LBB0_84

.LBB0_93:
	s_or_b64 exec, exec, s[8:9]
	s_waitcnt vmcnt(0)
	s_waitcnt vmcnt(0)

.LBB0_111:
	s_or_b64 exec, exec, s[0:1]
	s_mov_b64 s[0:1], exec
	v_mbcnt_lo_u32_b32 v2, s0, 0
	v_mbcnt_hi_u32_b32 v2, s1, v2
	v_cmp_eq_u32_e32 vcc, 0, v2
	s_waitcnt vmcnt(0)
	s_and_saveexec_b64 s[4:5], vcc
	s_cbranch_execz .LBB0_113
	s_bcnt1_i32_b64 s0, s[0:1]
	v_mov_b32_e32 v2, s0
	global_atomic_add v199, v2, s[6:7] offset:1024

.LBB0_449:
	s_or_b64 exec, exec, s[8:9]
	buffer_inv sc1
	v_cvt_f32_u32_e32 v6, v4
	s_waitcnt vmcnt(0)
	v_readfirstlane_b32 s0, v5
	v_sub_u32_e32 v5, 0, v4
	v_rcp_iflag_f32_e32 v6, v6
	v_add_u32_e32 v7, s0, v3
	v_mul_f32_e32 v6, 0x4f7ffffe, v6
	v_cvt_u32_f32_e32 v6, v6
	v_mul_lo_u32 v3, v5, v6
	v_mul_hi_u32 v3, v6, v3
	v_add_u32_e32 v3, v6, v3
	v_mul_hi_u32 v3, v7, v3
	v_mul_lo_u32 v5, v3, v4
	v_sub_u32_e32 v5, v7, v5
	v_add_u32_e32 v6, 1, v3
	v_cmp_ge_u32_e32 vcc, v5, v4
	s_nop 1
	v_cndmask_b32_e32 v3, v3, v6, vcc
	v_sub_u32_e32 v6, v5, v4
	v_cndmask_b32_e32 v5, v5, v6, vcc
	v_add_u32_e32 v6, 1, v3
	v_cmp_ge_u32_e32 vcc, v5, v4
	v_add_u32_e32 v5, 1, v7
	s_nop 0
	v_cndmask_b32_e32 v3, v3, v6, vcc
	v_mul_lo_u32 v6, v4, v3
	v_add_u32_e32 v4, v6, v4
	v_cmp_ne_u32_e32 vcc, v5, v4
	s_and_saveexec_b64 s[0:1], vcc
	s_xor_b64 s[0:1], exec, s[0:1]
	s_cbranch_execz .LBB0_463
	s_waitcnt lgkmcnt(0)
	global_load_dword v2, v199, s[6:7] offset:1024 sc1
	s_add_u32 s10, s6, 0x2400
	s_addc_u32 s11, s7, 0
	s_waitcnt vmcnt(0)
	v_cmp_eq_u32_e32 vcc, v2, v3
	s_and_saveexec_b64 s[8:9], vcc
	s_cbranch_execz .LBB0_462
	s_mov_b32 s22, 1
	s_mov_b64 s[12:13], 0
	s_branch .LBB0_453
